# grid barrier poll loops: s_sleep 1 between polls removed (tighter polling)
# speedup vs baseline: 1.0022x; 1.0022x over previous
.LBB0_111:
	global_load_dword v16, v17, s[54:55] offset:1024 sc1
	global_load_dword v1, v17, s[54:55] offset:1280 sc1
	global_load_dword v2, v17, s[54:55] offset:1536 sc1
	global_load_dword v3, v17, s[54:55] offset:1792 sc1
	global_load_dword v4, v17, s[54:55] offset:2048 sc1
	global_load_dword v5, v17, s[54:55] offset:2304 sc1
	global_load_dword v6, v17, s[54:55] offset:2560 sc1
	global_load_dword v7, v17, s[54:55] offset:2816 sc1
	global_load_dword v8, v17, s[54:55] offset:3072 sc1
	global_load_dword v9, v17, s[54:55] offset:3328 sc1
	global_load_dword v10, v17, s[54:55] offset:3584 sc1
	global_load_dword v11, v17, s[54:55] offset:3840 sc1
	global_load_dword v12, v17, s[4:5] sc1
	global_load_dword v13, v17, s[6:7] sc1
	global_load_dword v14, v17, s[8:9] sc1
	global_load_dword v15, v17, s[10:11] sc1
	s_mov_b64 s[12:13], -1
	s_mov_b64 s[14:15], -1
	s_waitcnt vmcnt(14)
	v_add_u32_e32 v18, v1, v16
	s_waitcnt vmcnt(13)
	v_add_u32_e32 v18, v18, v2
	s_waitcnt vmcnt(12)
	v_add_u32_e32 v18, v18, v3
	s_waitcnt vmcnt(11)
	v_add_u32_e32 v18, v18, v4
	s_waitcnt vmcnt(10)
	v_add_u32_e32 v18, v18, v5
	s_waitcnt vmcnt(9)
	v_add_u32_e32 v18, v18, v6
	s_waitcnt vmcnt(8)
	v_add_u32_e32 v18, v18, v7
	s_waitcnt vmcnt(7)
	v_add_u32_e32 v18, v18, v8
	s_waitcnt vmcnt(6)
	v_add_u32_e32 v18, v18, v9
	s_waitcnt vmcnt(5)
	v_add_u32_e32 v18, v18, v10
	s_waitcnt vmcnt(4)
	v_add_u32_e32 v18, v18, v11
	s_waitcnt vmcnt(3)
	v_add_u32_e32 v18, v18, v12
	s_waitcnt vmcnt(2)
	v_add_u32_e32 v18, v18, v13
	s_waitcnt vmcnt(1)
	v_add_u32_e32 v18, v18, v14
	s_waitcnt vmcnt(0)
	v_add_u32_e32 v18, v18, v15
	v_cmp_eq_u32_e32 vcc, s18, v18
	s_cbranch_vccnz .LBB0_110
	s_and_b32 s12, s19, 0xff
	s_cmp_eq_u32 s12, 0
	s_mov_b64 s[12:13], -1
	s_mov_b64 s[16:17], -1
	s_cbranch_scc1 .LBB0_115
	s_and_b64 vcc, exec, s[16:17]
	s_cbranch_vccz .LBB0_110

.LBB0_129:
	s_and_b32 s16, s20, 0xff
	s_mov_b64 s[14:15], -1
	s_cmp_lg_u32 s16, 0
	s_mov_b64 s[18:19], -1
	s_cbranch_scc0 .LBB0_132
	s_and_b64 vcc, exec, s[18:19]
	s_cbranch_vccz .LBB0_128

.LBB0_146:
	s_and_b32 s16, s22, 0xff
	s_cmp_lg_u32 s16, 0
	s_mov_b64 s[18:19], -1
	s_cbranch_scc0 .LBB0_149
	s_mov_b64 s[20:21], -1
	s_and_b64 vcc, exec, s[18:19]
	s_cbranch_vccz .LBB0_145

.LBB0_210:
	global_load_dword v17, v227, s[54:55] offset:1024 sc1
	global_load_dword v2, v227, s[54:55] offset:1280 sc1
	global_load_dword v3, v227, s[54:55] offset:1536 sc1
	global_load_dword v4, v227, s[54:55] offset:1792 sc1
	global_load_dword v5, v227, s[54:55] offset:2048 sc1
	global_load_dword v6, v227, s[54:55] offset:2304 sc1
	global_load_dword v7, v227, s[54:55] offset:2560 sc1
	global_load_dword v8, v227, s[54:55] offset:2816 sc1
	global_load_dword v9, v227, s[54:55] offset:3072 sc1
	global_load_dword v10, v227, s[54:55] offset:3328 sc1
	global_load_dword v11, v227, s[54:55] offset:3584 sc1
	global_load_dword v12, v227, s[54:55] offset:3840 sc1
	global_load_dword v13, v227, s[60:61] sc1
	global_load_dword v14, v227, s[62:63] sc1
	global_load_dword v15, v227, s[64:65] sc1
	global_load_dword v16, v227, s[66:67] sc1
	s_mov_b64 s[4:5], -1
	s_mov_b64 s[6:7], -1
	s_waitcnt vmcnt(14)
	v_add_u32_e32 v18, v2, v17
	s_waitcnt vmcnt(13)
	v_add_u32_e32 v18, v18, v3
	s_waitcnt vmcnt(12)
	v_add_u32_e32 v18, v18, v4
	s_waitcnt vmcnt(11)
	v_add_u32_e32 v18, v18, v5
	s_waitcnt vmcnt(10)
	v_add_u32_e32 v18, v18, v6
	s_waitcnt vmcnt(9)
	v_add_u32_e32 v18, v18, v7
	s_waitcnt vmcnt(8)
	v_add_u32_e32 v18, v18, v8
	s_waitcnt vmcnt(7)
	v_add_u32_e32 v18, v18, v9
	s_waitcnt vmcnt(6)
	v_add_u32_e32 v18, v18, v10
	s_waitcnt vmcnt(5)
	v_add_u32_e32 v18, v18, v11
	s_waitcnt vmcnt(4)
	v_add_u32_e32 v18, v18, v12
	s_waitcnt vmcnt(3)
	v_add_u32_e32 v18, v18, v13
	s_waitcnt vmcnt(2)
	v_add_u32_e32 v18, v18, v14
	s_waitcnt vmcnt(1)
	v_add_u32_e32 v18, v18, v15
	s_waitcnt vmcnt(0)
	v_add_u32_e32 v18, v18, v16
	v_cmp_eq_u32_e32 vcc, s11, v18
	s_cbranch_vccnz .LBB0_209
	s_and_b32 s4, s12, 0xff
	s_cmp_eq_u32 s4, 0
	s_mov_b64 s[4:5], -1
	s_mov_b64 s[8:9], -1
	s_cbranch_scc1 .LBB0_214
	s_and_b64 vcc, exec, s[8:9]
	s_cbranch_vccz .LBB0_209

.LBB0_228:
	s_and_b32 s16, s21, 0xff
	s_mov_b64 s[14:15], -1
	s_cmp_lg_u32 s16, 0
	s_mov_b64 s[18:19], -1
	s_cbranch_scc0 .LBB0_231
	s_and_b64 vcc, exec, s[18:19]
	s_cbranch_vccz .LBB0_227

.LBB0_245:
	s_and_b32 s14, s18, 0xff
	s_mov_b64 s[12:13], -1
	s_cmp_lg_u32 s14, 0
	s_mov_b64 s[16:17], -1
	s_cbranch_scc0 .LBB0_248
	s_and_b64 vcc, exec, s[16:17]
	s_cbranch_vccz .LBB0_244
